# v101 + out-proj K-loop LDS-DMAs with SGPR base + 32-bit lane offset as well
# baseline (speedup 1.0000x reference)
.LBB0_1201:
	s_ashr_i32 s53, s52, 31
	s_lshl_b64 s[26:27], s[52:53], 21
	s_add_u32 s72, s38, s26
	s_addc_u32 s73, s40, s27
	s_and_b64 s[26:27], s[4:5], exec
	s_cselect_b32 s35, s73, s7
	s_cselect_b32 s53, s72, s6
	s_ashr_i32 s31, s30, 31
	s_lshl_b64 s[26:27], s[30:31], 21
	s_add_u32 s74, s42, s26
	s_addc_u32 s75, s44, s27
	s_and_b64 s[26:27], s[4:5], exec
	s_cselect_b32 s31, s75, s25
	s_cselect_b32 s92, s74, s24
	s_add_u32 s6, s6, 0x100080
	s_addc_u32 s7, s7, 0
	s_add_u32 s21, s24, 0x100
	s_addc_u32 s13, s25, 0
	s_mov_b32 s58, -2
	s_waitcnt lgkmcnt(0)
	s_add_u32 s24, s6, 0xfff00080
	s_addc_u32 s25, s7, -1
	s_add_i32 s28, 0, 0x10000
	s_cmp_eq_u32 s58, 60
	s_cselect_b32 s27, s35, s25
	s_cselect_b32 s26, s53, s24
	s_cselect_b32 s25, s31, s13
	s_cselect_b32 s24, s92, s21
	s_add_i32 s71, 0, 0x14000
	v_add_u32_e32 v150, s28, v163
	v_add_u32_e32 v154, s71, v163
	ds_read_b128 v[138:141], v150
	ds_read_b128 v[142:145], v150 offset:1024
	ds_read_b128 v[146:149], v150 offset:2048
	ds_read_b128 v[150:153], v150 offset:3072
	ds_read_b128 v[168:171], v154
	ds_read_b128 v[172:175], v154 offset:1024
	ds_read_b128 v[176:179], v154 offset:2048
	ds_read_b128 v[180:183], v154 offset:3072
	s_add_i32 m0, s50, 0xc000
	ds_read_b128 v[188:191], v186
	ds_read_b128 v[192:195], v186 offset:1024
	ds_read_b128 v[196:199], v186 offset:2048
	ds_read_b128 v[200:203], v186 offset:3072
	ds_read_b128 v[222:225], v186 offset:4096
	ds_read_b128 v[226:229], v186 offset:5120
	ds_read_b128 v[230:233], v186 offset:6144
	ds_read_b128 v[234:237], v186 offset:7168
	global_load_lds_dwordx4 v134, s[6:7]
	s_add_i32 m0, s50, 0xe000
	s_nop 0
	global_load_lds_dwordx4 v136, s[6:7]
	s_waitcnt vmcnt(8)
	s_waitcnt lgkmcnt(0)
	s_setprio 1
	s_barrier
	v_mfma_f32_16x16x32_bf16 v[128:131], v[138:141], v[188:191], 0
	v_mfma_f32_16x16x32_bf16 v[124:127], v[146:149], v[188:191], 0
	v_mfma_f32_16x16x32_bf16 v[112:115], v[138:141], v[196:199], 0
	v_mfma_f32_16x16x32_bf16 v[108:111], v[146:149], v[196:199], 0
	v_mfma_f32_16x16x32_bf16 v[96:99], v[138:141], v[222:225], 0
	v_mfma_f32_16x16x32_bf16 v[92:95], v[146:149], v[222:225], 0
	v_mfma_f32_16x16x32_bf16 v[80:83], v[138:141], v[230:233], 0
	v_mfma_f32_16x16x32_bf16 v[76:79], v[146:149], v[230:233], 0
	v_mfma_f32_16x16x32_bf16 v[128:131], v[142:145], v[192:195], v[128:131]
	v_mfma_f32_16x16x32_bf16 v[124:127], v[150:153], v[192:195], v[124:127]
	v_mfma_f32_16x16x32_bf16 v[112:115], v[142:145], v[200:203], v[112:115]
	v_mfma_f32_16x16x32_bf16 v[108:111], v[150:153], v[200:203], v[108:111]
	v_mfma_f32_16x16x32_bf16 v[96:99], v[142:145], v[226:229], v[96:99]
	v_mfma_f32_16x16x32_bf16 v[92:95], v[150:153], v[226:229], v[92:95]
	v_mfma_f32_16x16x32_bf16 v[80:83], v[142:145], v[234:237], v[80:83]
	v_mfma_f32_16x16x32_bf16 v[76:79], v[150:153], v[234:237], v[76:79]
	v_mfma_f32_16x16x32_bf16 v[120:123], v[168:171], v[188:191], 0
	v_mfma_f32_16x16x32_bf16 v[116:119], v[176:179], v[188:191], 0
	v_mfma_f32_16x16x32_bf16 v[104:107], v[168:171], v[196:199], 0
	v_mfma_f32_16x16x32_bf16 v[100:103], v[176:179], v[196:199], 0
	v_mfma_f32_16x16x32_bf16 v[88:91], v[168:171], v[222:225], 0
	v_mfma_f32_16x16x32_bf16 v[84:87], v[176:179], v[222:225], 0
	v_mfma_f32_16x16x32_bf16 v[72:75], v[168:171], v[230:233], 0
	v_mfma_f32_16x16x32_bf16 v[68:71], v[176:179], v[230:233], 0
	v_mfma_f32_16x16x32_bf16 v[120:123], v[172:175], v[192:195], v[120:123]
	v_mfma_f32_16x16x32_bf16 v[116:119], v[180:183], v[192:195], v[116:119]
	v_mfma_f32_16x16x32_bf16 v[104:107], v[172:175], v[200:203], v[104:107]
	v_mfma_f32_16x16x32_bf16 v[100:103], v[180:183], v[200:203], v[100:103]
	v_mfma_f32_16x16x32_bf16 v[88:91], v[172:175], v[226:229], v[88:91]
	v_mfma_f32_16x16x32_bf16 v[84:87], v[180:183], v[226:229], v[84:87]
	v_mfma_f32_16x16x32_bf16 v[72:75], v[172:175], v[234:237], v[72:75]
	v_mfma_f32_16x16x32_bf16 v[68:71], v[180:183], v[234:237], v[68:71]
	s_barrier
	s_setprio 0
	s_add_i32 s28, s28, s46
	s_mov_b32 m0, s28
	ds_read_b128 v[188:191], v186 offset:16384
	ds_read_b128 v[192:195], v186 offset:17408
	ds_read_b128 v[196:199], v186 offset:18432
	ds_read_b128 v[200:203], v186 offset:19456
	ds_read_b128 v[222:225], v186 offset:20480
	ds_read_b128 v[226:229], v186 offset:21504
	ds_read_b128 v[230:233], v186 offset:22528
	ds_read_b128 v[234:237], v186 offset:23552
	global_load_lds_dwordx4 v2, s[24:25]
	s_add_i32 m0, s28, 0x2000
	s_add_u32 s28, s24, 0x100000
	s_addc_u32 s29, s25, 0
	s_add_i32 s71, s71, s46
	global_load_lds_dwordx4 v132, s[24:25]
	s_mov_b32 m0, s71
	s_nop 0
	global_load_lds_dwordx4 v2, s[28:29]
	s_add_i32 m0, s71, 0x2000
	s_nop 0
	global_load_lds_dwordx4 v132, s[28:29]
	s_mov_b32 m0, s50
	s_nop 0
	global_load_lds_dwordx4 v2, s[26:27]
	s_mov_b32 m0, s23
	s_nop 0
	global_load_lds_dwordx4 v132, s[26:27]
	s_waitcnt vmcnt(8)
	s_waitcnt lgkmcnt(0)
	s_setprio 1
	s_barrier
	v_mfma_f32_16x16x32_bf16 v[64:67], v[138:141], v[188:191], 0
	v_mfma_f32_16x16x32_bf16 v[60:63], v[146:149], v[188:191], 0
	v_mfma_f32_16x16x32_bf16 v[48:51], v[138:141], v[196:199], 0
	v_mfma_f32_16x16x32_bf16 v[44:47], v[146:149], v[196:199], 0
	v_mfma_f32_16x16x32_bf16 v[32:35], v[138:141], v[222:225], 0
	v_mfma_f32_16x16x32_bf16 v[28:31], v[146:149], v[222:225], 0
	v_mfma_f32_16x16x32_bf16 v[16:19], v[138:141], v[230:233], 0
	v_mfma_f32_16x16x32_bf16 v[12:15], v[146:149], v[230:233], 0
	v_mfma_f32_16x16x32_bf16 v[64:67], v[142:145], v[192:195], v[64:67]
	v_mfma_f32_16x16x32_bf16 v[60:63], v[150:153], v[192:195], v[60:63]
	v_mfma_f32_16x16x32_bf16 v[48:51], v[142:145], v[200:203], v[48:51]
	v_mfma_f32_16x16x32_bf16 v[44:47], v[150:153], v[200:203], v[44:47]
	v_mfma_f32_16x16x32_bf16 v[32:35], v[142:145], v[226:229], v[32:35]
	v_mfma_f32_16x16x32_bf16 v[28:31], v[150:153], v[226:229], v[28:31]
	v_mfma_f32_16x16x32_bf16 v[16:19], v[142:145], v[234:237], v[16:19]
	v_mfma_f32_16x16x32_bf16 v[12:15], v[150:153], v[234:237], v[12:15]
	v_mfma_f32_16x16x32_bf16 v[56:59], v[168:171], v[188:191], 0
	v_mfma_f32_16x16x32_bf16 v[52:55], v[176:179], v[188:191], 0
	v_mfma_f32_16x16x32_bf16 v[40:43], v[168:171], v[196:199], 0
	v_mfma_f32_16x16x32_bf16 v[36:39], v[176:179], v[196:199], 0
	v_mfma_f32_16x16x32_bf16 v[24:27], v[168:171], v[222:225], 0
	v_mfma_f32_16x16x32_bf16 v[20:23], v[176:179], v[222:225], 0
	v_mfma_f32_16x16x32_bf16 v[8:11], v[168:171], v[230:233], 0
	v_mfma_f32_16x16x32_bf16 v[4:7], v[176:179], v[230:233], 0
	v_mfma_f32_16x16x32_bf16 v[56:59], v[172:175], v[192:195], v[56:59]
	v_mfma_f32_16x16x32_bf16 v[52:55], v[180:183], v[192:195], v[52:55]
	v_mfma_f32_16x16x32_bf16 v[40:43], v[172:175], v[200:203], v[40:43]
	v_mfma_f32_16x16x32_bf16 v[36:39], v[180:183], v[200:203], v[36:39]
	v_mfma_f32_16x16x32_bf16 v[24:27], v[172:175], v[226:229], v[24:27]
	v_mfma_f32_16x16x32_bf16 v[20:23], v[180:183], v[226:229], v[20:23]
	v_mfma_f32_16x16x32_bf16 v[8:11], v[172:175], v[234:237], v[8:11]
	v_mfma_f32_16x16x32_bf16 v[4:7], v[180:183], v[234:237], v[4:7]
	s_barrier
	s_setprio 0
	s_add_i32 s28, 0, 0x18000
	s_add_i32 s29, 0, 0x1c000
	v_add_u32_e32 v150, s28, v163
	v_add_u32_e32 v180, s29, v163
	ds_read_b128 v[138:141], v150
	ds_read_b128 v[142:145], v150 offset:1024
	ds_read_b128 v[146:149], v150 offset:2048
	ds_read_b128 v[150:153], v150 offset:3072
	ds_read_b128 v[168:171], v180
	ds_read_b128 v[172:175], v180 offset:1024
	ds_read_b128 v[176:179], v180 offset:2048
	ds_read_b128 v[180:183], v180 offset:3072
	s_add_u32 s100, s26, 0x80
	s_addc_u32 s101, s27, 0
	s_add_u32 s26, s26, 0x100000
	s_addc_u32 s27, s27, 0
	s_mov_b32 m0, s51
	ds_read_b128 v[188:191], v186 offset:32768
	ds_read_b128 v[192:195], v186 offset:33792
	ds_read_b128 v[196:199], v186 offset:34816
	ds_read_b128 v[200:203], v186 offset:35840
	ds_read_b128 v[222:225], v186 offset:36864
	ds_read_b128 v[226:229], v186 offset:37888
	ds_read_b128 v[230:233], v186 offset:38912
	ds_read_b128 v[234:237], v186 offset:39936
	global_load_lds_dwordx4 v2, s[26:27]
	s_mov_b32 m0, s54
	s_nop 0
	global_load_lds_dwordx4 v132, s[26:27]
	s_waitcnt vmcnt(8)
	s_waitcnt lgkmcnt(0)
	s_setprio 1
	s_barrier
	v_mfma_f32_16x16x32_bf16 v[128:131], v[138:141], v[188:191], v[128:131]
	v_mfma_f32_16x16x32_bf16 v[124:127], v[146:149], v[188:191], v[124:127]
	v_mfma_f32_16x16x32_bf16 v[112:115], v[138:141], v[196:199], v[112:115]
	v_mfma_f32_16x16x32_bf16 v[108:111], v[146:149], v[196:199], v[108:111]
	v_mfma_f32_16x16x32_bf16 v[96:99], v[138:141], v[222:225], v[96:99]
	v_mfma_f32_16x16x32_bf16 v[92:95], v[146:149], v[222:225], v[92:95]
	v_mfma_f32_16x16x32_bf16 v[80:83], v[138:141], v[230:233], v[80:83]
	v_mfma_f32_16x16x32_bf16 v[76:79], v[146:149], v[230:233], v[76:79]
	v_mfma_f32_16x16x32_bf16 v[128:131], v[142:145], v[192:195], v[128:131]
	v_mfma_f32_16x16x32_bf16 v[124:127], v[150:153], v[192:195], v[124:127]
	v_mfma_f32_16x16x32_bf16 v[112:115], v[142:145], v[200:203], v[112:115]
	v_mfma_f32_16x16x32_bf16 v[108:111], v[150:153], v[200:203], v[108:111]
	v_mfma_f32_16x16x32_bf16 v[96:99], v[142:145], v[226:229], v[96:99]
	v_mfma_f32_16x16x32_bf16 v[92:95], v[150:153], v[226:229], v[92:95]
	v_mfma_f32_16x16x32_bf16 v[80:83], v[142:145], v[234:237], v[80:83]
	v_mfma_f32_16x16x32_bf16 v[76:79], v[150:153], v[234:237], v[76:79]
	v_mfma_f32_16x16x32_bf16 v[120:123], v[168:171], v[188:191], v[120:123]
	v_mfma_f32_16x16x32_bf16 v[116:119], v[176:179], v[188:191], v[116:119]
	v_mfma_f32_16x16x32_bf16 v[104:107], v[168:171], v[196:199], v[104:107]
	v_mfma_f32_16x16x32_bf16 v[100:103], v[176:179], v[196:199], v[100:103]
	v_mfma_f32_16x16x32_bf16 v[88:91], v[168:171], v[222:225], v[88:91]
	v_mfma_f32_16x16x32_bf16 v[84:87], v[176:179], v[222:225], v[84:87]
	v_mfma_f32_16x16x32_bf16 v[72:75], v[168:171], v[230:233], v[72:75]
	v_mfma_f32_16x16x32_bf16 v[68:71], v[176:179], v[230:233], v[68:71]
	v_mfma_f32_16x16x32_bf16 v[120:123], v[172:175], v[192:195], v[120:123]
	v_mfma_f32_16x16x32_bf16 v[116:119], v[180:183], v[192:195], v[116:119]
	v_mfma_f32_16x16x32_bf16 v[104:107], v[172:175], v[200:203], v[104:107]
	v_mfma_f32_16x16x32_bf16 v[100:103], v[180:183], v[200:203], v[100:103]
	v_mfma_f32_16x16x32_bf16 v[88:91], v[172:175], v[226:229], v[88:91]
	v_mfma_f32_16x16x32_bf16 v[84:87], v[180:183], v[226:229], v[84:87]
	v_mfma_f32_16x16x32_bf16 v[72:75], v[172:175], v[234:237], v[72:75]
	v_mfma_f32_16x16x32_bf16 v[68:71], v[180:183], v[234:237], v[68:71]
	s_barrier
	s_setprio 0
	s_add_i32 s26, s28, s46
	s_add_u32 s24, s24, 0x80
	s_addc_u32 s25, s25, 0
	s_mov_b32 m0, s26
	ds_read_b128 v[188:191], v186 offset:49152
	ds_read_b128 v[192:195], v186 offset:50176
	ds_read_b128 v[196:199], v186 offset:51200
	ds_read_b128 v[200:203], v186 offset:52224
	ds_read_b128 v[222:225], v186 offset:53248
	ds_read_b128 v[226:229], v186 offset:54272
	ds_read_b128 v[230:233], v186 offset:55296
	ds_read_b128 v[234:237], v186 offset:56320
	global_load_lds_dwordx4 v2, s[24:25]
	s_add_i32 m0, s26, 0x2000
	s_add_i32 s26, s29, s46
	global_load_lds_dwordx4 v132, s[24:25]
	s_add_u32 s24, s24, 0x100000
	s_addc_u32 s25, s25, 0
	s_mov_b32 m0, s26
	s_nop 0
	global_load_lds_dwordx4 v2, s[24:25]
	s_add_i32 m0, s26, 0x2000
	s_nop 0
	global_load_lds_dwordx4 v132, s[24:25]
	s_mov_b32 m0, s76
	s_nop 0
	global_load_lds_dwordx4 v2, s[100:101]
	s_mov_b32 m0, s77
	s_nop 0
	global_load_lds_dwordx4 v132, s[100:101]
	s_waitcnt vmcnt(8)
	s_waitcnt lgkmcnt(0)
	s_setprio 1
	s_barrier
	v_mfma_f32_16x16x32_bf16 v[64:67], v[138:141], v[188:191], v[64:67]
	v_mfma_f32_16x16x32_bf16 v[60:63], v[146:149], v[188:191], v[60:63]
	v_mfma_f32_16x16x32_bf16 v[48:51], v[138:141], v[196:199], v[48:51]
	v_mfma_f32_16x16x32_bf16 v[44:47], v[146:149], v[196:199], v[44:47]
	v_mfma_f32_16x16x32_bf16 v[32:35], v[138:141], v[222:225], v[32:35]
	v_mfma_f32_16x16x32_bf16 v[28:31], v[146:149], v[222:225], v[28:31]
	v_mfma_f32_16x16x32_bf16 v[16:19], v[138:141], v[230:233], v[16:19]
	v_mfma_f32_16x16x32_bf16 v[12:15], v[146:149], v[230:233], v[12:15]
	v_mfma_f32_16x16x32_bf16 v[64:67], v[142:145], v[192:195], v[64:67]
	v_mfma_f32_16x16x32_bf16 v[60:63], v[150:153], v[192:195], v[60:63]
	v_mfma_f32_16x16x32_bf16 v[48:51], v[142:145], v[200:203], v[48:51]
	v_mfma_f32_16x16x32_bf16 v[44:47], v[150:153], v[200:203], v[44:47]
	v_mfma_f32_16x16x32_bf16 v[32:35], v[142:145], v[226:229], v[32:35]
	v_mfma_f32_16x16x32_bf16 v[28:31], v[150:153], v[226:229], v[28:31]
	v_mfma_f32_16x16x32_bf16 v[16:19], v[142:145], v[234:237], v[16:19]
	v_mfma_f32_16x16x32_bf16 v[12:15], v[150:153], v[234:237], v[12:15]
	v_mfma_f32_16x16x32_bf16 v[56:59], v[168:171], v[188:191], v[56:59]
	v_mfma_f32_16x16x32_bf16 v[52:55], v[176:179], v[188:191], v[52:55]
	v_mfma_f32_16x16x32_bf16 v[40:43], v[168:171], v[196:199], v[40:43]
	v_mfma_f32_16x16x32_bf16 v[36:39], v[176:179], v[196:199], v[36:39]
	v_mfma_f32_16x16x32_bf16 v[24:27], v[168:171], v[222:225], v[24:27]
	v_mfma_f32_16x16x32_bf16 v[20:23], v[176:179], v[222:225], v[20:23]
	v_mfma_f32_16x16x32_bf16 v[8:11], v[168:171], v[230:233], v[8:11]
	v_mfma_f32_16x16x32_bf16 v[4:7], v[176:179], v[230:233], v[4:7]
	v_mfma_f32_16x16x32_bf16 v[56:59], v[172:175], v[192:195], v[56:59]
	v_mfma_f32_16x16x32_bf16 v[52:55], v[180:183], v[192:195], v[52:55]
	v_mfma_f32_16x16x32_bf16 v[40:43], v[172:175], v[200:203], v[40:43]
	v_mfma_f32_16x16x32_bf16 v[36:39], v[180:183], v[200:203], v[36:39]
	v_mfma_f32_16x16x32_bf16 v[24:27], v[172:175], v[226:229], v[24:27]
	v_mfma_f32_16x16x32_bf16 v[20:23], v[180:183], v[226:229], v[20:23]
	v_mfma_f32_16x16x32_bf16 v[8:11], v[172:175], v[234:237], v[8:11]
	v_mfma_f32_16x16x32_bf16 v[4:7], v[180:183], v[234:237], v[4:7]
	s_barrier
	s_setprio 0
	s_add_i32 s58, s58, 2
	s_add_u32 s6, s6, 0x100
	s_addc_u32 s7, s7, 0
	s_add_u32 s21, s21, 0x100
	s_addc_u32 s13, s13, 0
	s_cmp_gt_u32 s58, 61
	s_cbranch_scc0 .LBB0_1202
.LBB0_1202:
	s_add_u32 s24, s6, 0xfff00080
	s_addc_u32 s25, s7, -1
	s_add_i32 s28, 0, 0x10000
	s_cmp_eq_u32 s58, 60
	s_cselect_b32 s27, s35, s25
	s_cselect_b32 s26, s53, s24
	s_cselect_b32 s25, s31, s13
	s_cselect_b32 s24, s92, s21
	s_add_i32 s71, 0, 0x14000
	v_add_u32_e32 v150, s28, v163
	v_add_u32_e32 v154, s71, v163
	ds_read_b128 v[138:141], v150
	ds_read_b128 v[142:145], v150 offset:1024
	ds_read_b128 v[146:149], v150 offset:2048
	ds_read_b128 v[150:153], v150 offset:3072
	ds_read_b128 v[168:171], v154
	ds_read_b128 v[172:175], v154 offset:1024
	ds_read_b128 v[176:179], v154 offset:2048
	ds_read_b128 v[180:183], v154 offset:3072
	s_add_i32 m0, s50, 0xc000
	ds_read_b128 v[188:191], v186
	ds_read_b128 v[192:195], v186 offset:1024
	ds_read_b128 v[196:199], v186 offset:2048
	ds_read_b128 v[200:203], v186 offset:3072
	ds_read_b128 v[222:225], v186 offset:4096
	ds_read_b128 v[226:229], v186 offset:5120
	ds_read_b128 v[230:233], v186 offset:6144
	ds_read_b128 v[234:237], v186 offset:7168
	global_load_lds_dwordx4 v134, s[6:7]
	s_add_i32 m0, s50, 0xe000
	s_nop 0
	global_load_lds_dwordx4 v136, s[6:7]
	s_waitcnt vmcnt(8)
	s_waitcnt lgkmcnt(0)
	s_setprio 1
	s_barrier
	v_mfma_f32_16x16x32_bf16 v[128:131], v[138:141], v[188:191], v[128:131]
	v_mfma_f32_16x16x32_bf16 v[124:127], v[146:149], v[188:191], v[124:127]
	v_mfma_f32_16x16x32_bf16 v[112:115], v[138:141], v[196:199], v[112:115]
	v_mfma_f32_16x16x32_bf16 v[108:111], v[146:149], v[196:199], v[108:111]
	v_mfma_f32_16x16x32_bf16 v[96:99], v[138:141], v[222:225], v[96:99]
	v_mfma_f32_16x16x32_bf16 v[92:95], v[146:149], v[222:225], v[92:95]
	v_mfma_f32_16x16x32_bf16 v[80:83], v[138:141], v[230:233], v[80:83]
	v_mfma_f32_16x16x32_bf16 v[76:79], v[146:149], v[230:233], v[76:79]
	v_mfma_f32_16x16x32_bf16 v[128:131], v[142:145], v[192:195], v[128:131]
	v_mfma_f32_16x16x32_bf16 v[124:127], v[150:153], v[192:195], v[124:127]
	v_mfma_f32_16x16x32_bf16 v[112:115], v[142:145], v[200:203], v[112:115]
	v_mfma_f32_16x16x32_bf16 v[108:111], v[150:153], v[200:203], v[108:111]
	v_mfma_f32_16x16x32_bf16 v[96:99], v[142:145], v[226:229], v[96:99]
	v_mfma_f32_16x16x32_bf16 v[92:95], v[150:153], v[226:229], v[92:95]
	v_mfma_f32_16x16x32_bf16 v[80:83], v[142:145], v[234:237], v[80:83]
	v_mfma_f32_16x16x32_bf16 v[76:79], v[150:153], v[234:237], v[76:79]
	v_mfma_f32_16x16x32_bf16 v[120:123], v[168:171], v[188:191], v[120:123]
	v_mfma_f32_16x16x32_bf16 v[116:119], v[176:179], v[188:191], v[116:119]
	v_mfma_f32_16x16x32_bf16 v[104:107], v[168:171], v[196:199], v[104:107]
	v_mfma_f32_16x16x32_bf16 v[100:103], v[176:179], v[196:199], v[100:103]
	v_mfma_f32_16x16x32_bf16 v[88:91], v[168:171], v[222:225], v[88:91]
	v_mfma_f32_16x16x32_bf16 v[84:87], v[176:179], v[222:225], v[84:87]
	v_mfma_f32_16x16x32_bf16 v[72:75], v[168:171], v[230:233], v[72:75]
	v_mfma_f32_16x16x32_bf16 v[68:71], v[176:179], v[230:233], v[68:71]
	v_mfma_f32_16x16x32_bf16 v[120:123], v[172:175], v[192:195], v[120:123]
	v_mfma_f32_16x16x32_bf16 v[116:119], v[180:183], v[192:195], v[116:119]
	v_mfma_f32_16x16x32_bf16 v[104:107], v[172:175], v[200:203], v[104:107]
	v_mfma_f32_16x16x32_bf16 v[100:103], v[180:183], v[200:203], v[100:103]
	v_mfma_f32_16x16x32_bf16 v[88:91], v[172:175], v[226:229], v[88:91]
	v_mfma_f32_16x16x32_bf16 v[84:87], v[180:183], v[226:229], v[84:87]
	v_mfma_f32_16x16x32_bf16 v[72:75], v[172:175], v[234:237], v[72:75]
	v_mfma_f32_16x16x32_bf16 v[68:71], v[180:183], v[234:237], v[68:71]
	s_barrier
	s_setprio 0
	s_add_i32 s28, s28, s46
	s_mov_b32 m0, s28
	ds_read_b128 v[188:191], v186 offset:16384
	ds_read_b128 v[192:195], v186 offset:17408
	ds_read_b128 v[196:199], v186 offset:18432
	ds_read_b128 v[200:203], v186 offset:19456
	ds_read_b128 v[222:225], v186 offset:20480
	ds_read_b128 v[226:229], v186 offset:21504
	ds_read_b128 v[230:233], v186 offset:22528
	ds_read_b128 v[234:237], v186 offset:23552
	global_load_lds_dwordx4 v2, s[24:25]
	s_add_i32 m0, s28, 0x2000
	s_add_u32 s28, s24, 0x100000
	s_addc_u32 s29, s25, 0
	s_add_i32 s71, s71, s46
	global_load_lds_dwordx4 v132, s[24:25]
	s_mov_b32 m0, s71
	s_nop 0
	global_load_lds_dwordx4 v2, s[28:29]
	s_add_i32 m0, s71, 0x2000
	s_nop 0
	global_load_lds_dwordx4 v132, s[28:29]
	s_mov_b32 m0, s50
	s_nop 0
	global_load_lds_dwordx4 v2, s[26:27]
	s_mov_b32 m0, s23
	s_nop 0
	global_load_lds_dwordx4 v132, s[26:27]
	s_waitcnt vmcnt(8)
	s_waitcnt lgkmcnt(0)
	s_setprio 1
	s_barrier
	v_mfma_f32_16x16x32_bf16 v[64:67], v[138:141], v[188:191], v[64:67]
	v_mfma_f32_16x16x32_bf16 v[60:63], v[146:149], v[188:191], v[60:63]
	v_mfma_f32_16x16x32_bf16 v[48:51], v[138:141], v[196:199], v[48:51]
	v_mfma_f32_16x16x32_bf16 v[44:47], v[146:149], v[196:199], v[44:47]
	v_mfma_f32_16x16x32_bf16 v[32:35], v[138:141], v[222:225], v[32:35]
	v_mfma_f32_16x16x32_bf16 v[28:31], v[146:149], v[222:225], v[28:31]
	v_mfma_f32_16x16x32_bf16 v[16:19], v[138:141], v[230:233], v[16:19]
	v_mfma_f32_16x16x32_bf16 v[12:15], v[146:149], v[230:233], v[12:15]
	v_mfma_f32_16x16x32_bf16 v[64:67], v[142:145], v[192:195], v[64:67]
	v_mfma_f32_16x16x32_bf16 v[60:63], v[150:153], v[192:195], v[60:63]
	v_mfma_f32_16x16x32_bf16 v[48:51], v[142:145], v[200:203], v[48:51]
	v_mfma_f32_16x16x32_bf16 v[44:47], v[150:153], v[200:203], v[44:47]
	v_mfma_f32_16x16x32_bf16 v[32:35], v[142:145], v[226:229], v[32:35]
	v_mfma_f32_16x16x32_bf16 v[28:31], v[150:153], v[226:229], v[28:31]
	v_mfma_f32_16x16x32_bf16 v[16:19], v[142:145], v[234:237], v[16:19]
	v_mfma_f32_16x16x32_bf16 v[12:15], v[150:153], v[234:237], v[12:15]
	v_mfma_f32_16x16x32_bf16 v[56:59], v[168:171], v[188:191], v[56:59]
	v_mfma_f32_16x16x32_bf16 v[52:55], v[176:179], v[188:191], v[52:55]
	v_mfma_f32_16x16x32_bf16 v[40:43], v[168:171], v[196:199], v[40:43]
	v_mfma_f32_16x16x32_bf16 v[36:39], v[176:179], v[196:199], v[36:39]
	v_mfma_f32_16x16x32_bf16 v[24:27], v[168:171], v[222:225], v[24:27]
	v_mfma_f32_16x16x32_bf16 v[20:23], v[176:179], v[222:225], v[20:23]
	v_mfma_f32_16x16x32_bf16 v[8:11], v[168:171], v[230:233], v[8:11]
	v_mfma_f32_16x16x32_bf16 v[4:7], v[176:179], v[230:233], v[4:7]
	v_mfma_f32_16x16x32_bf16 v[56:59], v[172:175], v[192:195], v[56:59]
	v_mfma_f32_16x16x32_bf16 v[52:55], v[180:183], v[192:195], v[52:55]
	v_mfma_f32_16x16x32_bf16 v[40:43], v[172:175], v[200:203], v[40:43]
	v_mfma_f32_16x16x32_bf16 v[36:39], v[180:183], v[200:203], v[36:39]
	v_mfma_f32_16x16x32_bf16 v[24:27], v[172:175], v[226:229], v[24:27]
	v_mfma_f32_16x16x32_bf16 v[20:23], v[180:183], v[226:229], v[20:23]
	v_mfma_f32_16x16x32_bf16 v[8:11], v[172:175], v[234:237], v[8:11]
	v_mfma_f32_16x16x32_bf16 v[4:7], v[180:183], v[234:237], v[4:7]
	s_barrier
	s_setprio 0
	s_add_i32 s28, 0, 0x18000
	s_add_i32 s29, 0, 0x1c000
	v_add_u32_e32 v150, s28, v163
	v_add_u32_e32 v180, s29, v163
	ds_read_b128 v[138:141], v150
	ds_read_b128 v[142:145], v150 offset:1024
	ds_read_b128 v[146:149], v150 offset:2048
	ds_read_b128 v[150:153], v150 offset:3072
	ds_read_b128 v[168:171], v180
	ds_read_b128 v[172:175], v180 offset:1024
	ds_read_b128 v[176:179], v180 offset:2048
	ds_read_b128 v[180:183], v180 offset:3072
	s_add_u32 s100, s26, 0x80
	s_addc_u32 s101, s27, 0
	s_add_u32 s26, s26, 0x100000
	s_addc_u32 s27, s27, 0
	s_mov_b32 m0, s51
	ds_read_b128 v[188:191], v186 offset:32768
	ds_read_b128 v[192:195], v186 offset:33792
	ds_read_b128 v[196:199], v186 offset:34816
	ds_read_b128 v[200:203], v186 offset:35840
	ds_read_b128 v[222:225], v186 offset:36864
	ds_read_b128 v[226:229], v186 offset:37888
	ds_read_b128 v[230:233], v186 offset:38912
	ds_read_b128 v[234:237], v186 offset:39936
	global_load_lds_dwordx4 v2, s[26:27]
	s_mov_b32 m0, s54
	s_nop 0
	global_load_lds_dwordx4 v132, s[26:27]
	s_waitcnt vmcnt(8)
	s_waitcnt lgkmcnt(0)
	s_setprio 1
	s_barrier
	v_mfma_f32_16x16x32_bf16 v[128:131], v[138:141], v[188:191], v[128:131]
	v_mfma_f32_16x16x32_bf16 v[124:127], v[146:149], v[188:191], v[124:127]
	v_mfma_f32_16x16x32_bf16 v[112:115], v[138:141], v[196:199], v[112:115]
	v_mfma_f32_16x16x32_bf16 v[108:111], v[146:149], v[196:199], v[108:111]
	v_mfma_f32_16x16x32_bf16 v[96:99], v[138:141], v[222:225], v[96:99]
	v_mfma_f32_16x16x32_bf16 v[92:95], v[146:149], v[222:225], v[92:95]
	v_mfma_f32_16x16x32_bf16 v[80:83], v[138:141], v[230:233], v[80:83]
	v_mfma_f32_16x16x32_bf16 v[76:79], v[146:149], v[230:233], v[76:79]
	v_mfma_f32_16x16x32_bf16 v[128:131], v[142:145], v[192:195], v[128:131]
	v_mfma_f32_16x16x32_bf16 v[124:127], v[150:153], v[192:195], v[124:127]
	v_mfma_f32_16x16x32_bf16 v[112:115], v[142:145], v[200:203], v[112:115]
	v_mfma_f32_16x16x32_bf16 v[108:111], v[150:153], v[200:203], v[108:111]
	v_mfma_f32_16x16x32_bf16 v[96:99], v[142:145], v[226:229], v[96:99]
	v_mfma_f32_16x16x32_bf16 v[92:95], v[150:153], v[226:229], v[92:95]
	v_mfma_f32_16x16x32_bf16 v[80:83], v[142:145], v[234:237], v[80:83]
	v_mfma_f32_16x16x32_bf16 v[76:79], v[150:153], v[234:237], v[76:79]
	v_mfma_f32_16x16x32_bf16 v[120:123], v[168:171], v[188:191], v[120:123]
	v_mfma_f32_16x16x32_bf16 v[116:119], v[176:179], v[188:191], v[116:119]
	v_mfma_f32_16x16x32_bf16 v[104:107], v[168:171], v[196:199], v[104:107]
	v_mfma_f32_16x16x32_bf16 v[100:103], v[176:179], v[196:199], v[100:103]
	v_mfma_f32_16x16x32_bf16 v[88:91], v[168:171], v[222:225], v[88:91]
	v_mfma_f32_16x16x32_bf16 v[84:87], v[176:179], v[222:225], v[84:87]
	v_mfma_f32_16x16x32_bf16 v[72:75], v[168:171], v[230:233], v[72:75]
	v_mfma_f32_16x16x32_bf16 v[68:71], v[176:179], v[230:233], v[68:71]
	v_mfma_f32_16x16x32_bf16 v[120:123], v[172:175], v[192:195], v[120:123]
	v_mfma_f32_16x16x32_bf16 v[116:119], v[180:183], v[192:195], v[116:119]
	v_mfma_f32_16x16x32_bf16 v[104:107], v[172:175], v[200:203], v[104:107]
	v_mfma_f32_16x16x32_bf16 v[100:103], v[180:183], v[200:203], v[100:103]
	v_mfma_f32_16x16x32_bf16 v[88:91], v[172:175], v[226:229], v[88:91]
	v_mfma_f32_16x16x32_bf16 v[84:87], v[180:183], v[226:229], v[84:87]
	v_mfma_f32_16x16x32_bf16 v[72:75], v[172:175], v[234:237], v[72:75]
	v_mfma_f32_16x16x32_bf16 v[68:71], v[180:183], v[234:237], v[68:71]
	s_barrier
	s_setprio 0
	s_add_i32 s26, s28, s46
	s_add_u32 s24, s24, 0x80
	s_addc_u32 s25, s25, 0
	s_mov_b32 m0, s26
	ds_read_b128 v[188:191], v186 offset:49152
	ds_read_b128 v[192:195], v186 offset:50176
	ds_read_b128 v[196:199], v186 offset:51200
	ds_read_b128 v[200:203], v186 offset:52224
	ds_read_b128 v[222:225], v186 offset:53248
	ds_read_b128 v[226:229], v186 offset:54272
	ds_read_b128 v[230:233], v186 offset:55296
	ds_read_b128 v[234:237], v186 offset:56320
	global_load_lds_dwordx4 v2, s[24:25]
	s_add_i32 m0, s26, 0x2000
	s_add_i32 s26, s29, s46
	global_load_lds_dwordx4 v132, s[24:25]
	s_add_u32 s24, s24, 0x100000
	s_addc_u32 s25, s25, 0
	s_mov_b32 m0, s26
	s_nop 0
	global_load_lds_dwordx4 v2, s[24:25]
	s_add_i32 m0, s26, 0x2000
	s_nop 0
	global_load_lds_dwordx4 v132, s[24:25]
	s_mov_b32 m0, s76
	s_nop 0
	global_load_lds_dwordx4 v2, s[100:101]
	s_mov_b32 m0, s77
	s_nop 0
	global_load_lds_dwordx4 v132, s[100:101]
	s_waitcnt vmcnt(8)
	s_waitcnt lgkmcnt(0)
	s_setprio 1
	s_barrier
	v_mfma_f32_16x16x32_bf16 v[64:67], v[138:141], v[188:191], v[64:67]
	v_mfma_f32_16x16x32_bf16 v[60:63], v[146:149], v[188:191], v[60:63]
	v_mfma_f32_16x16x32_bf16 v[48:51], v[138:141], v[196:199], v[48:51]
	v_mfma_f32_16x16x32_bf16 v[44:47], v[146:149], v[196:199], v[44:47]
	v_mfma_f32_16x16x32_bf16 v[32:35], v[138:141], v[222:225], v[32:35]
	v_mfma_f32_16x16x32_bf16 v[28:31], v[146:149], v[222:225], v[28:31]
	v_mfma_f32_16x16x32_bf16 v[16:19], v[138:141], v[230:233], v[16:19]
	v_mfma_f32_16x16x32_bf16 v[12:15], v[146:149], v[230:233], v[12:15]
	v_mfma_f32_16x16x32_bf16 v[64:67], v[142:145], v[192:195], v[64:67]
	v_mfma_f32_16x16x32_bf16 v[60:63], v[150:153], v[192:195], v[60:63]
	v_mfma_f32_16x16x32_bf16 v[48:51], v[142:145], v[200:203], v[48:51]
	v_mfma_f32_16x16x32_bf16 v[44:47], v[150:153], v[200:203], v[44:47]
	v_mfma_f32_16x16x32_bf16 v[32:35], v[142:145], v[226:229], v[32:35]
	v_mfma_f32_16x16x32_bf16 v[28:31], v[150:153], v[226:229], v[28:31]
	v_mfma_f32_16x16x32_bf16 v[16:19], v[142:145], v[234:237], v[16:19]
	v_mfma_f32_16x16x32_bf16 v[12:15], v[150:153], v[234:237], v[12:15]
	v_mfma_f32_16x16x32_bf16 v[56:59], v[168:171], v[188:191], v[56:59]
	v_mfma_f32_16x16x32_bf16 v[52:55], v[176:179], v[188:191], v[52:55]
	v_mfma_f32_16x16x32_bf16 v[40:43], v[168:171], v[196:199], v[40:43]
	v_mfma_f32_16x16x32_bf16 v[36:39], v[176:179], v[196:199], v[36:39]
	v_mfma_f32_16x16x32_bf16 v[24:27], v[168:171], v[222:225], v[24:27]
	v_mfma_f32_16x16x32_bf16 v[20:23], v[176:179], v[222:225], v[20:23]
	v_mfma_f32_16x16x32_bf16 v[8:11], v[168:171], v[230:233], v[8:11]
	v_mfma_f32_16x16x32_bf16 v[4:7], v[176:179], v[230:233], v[4:7]
	v_mfma_f32_16x16x32_bf16 v[56:59], v[172:175], v[192:195], v[56:59]
	v_mfma_f32_16x16x32_bf16 v[52:55], v[180:183], v[192:195], v[52:55]
	v_mfma_f32_16x16x32_bf16 v[40:43], v[172:175], v[200:203], v[40:43]
	v_mfma_f32_16x16x32_bf16 v[36:39], v[180:183], v[200:203], v[36:39]
	v_mfma_f32_16x16x32_bf16 v[24:27], v[172:175], v[226:229], v[24:27]
	v_mfma_f32_16x16x32_bf16 v[20:23], v[180:183], v[226:229], v[20:23]
	v_mfma_f32_16x16x32_bf16 v[8:11], v[172:175], v[234:237], v[8:11]
	v_mfma_f32_16x16x32_bf16 v[4:7], v[180:183], v[234:237], v[4:7]
	s_barrier
	s_setprio 0
	s_add_i32 s58, s58, 2
	s_add_u32 s6, s6, 0x100
	s_addc_u32 s7, s7, 0
	s_add_u32 s21, s21, 0x100
	s_addc_u32 s13, s13, 0
	s_cmp_gt_u32 s58, 61
	s_cbranch_scc0 .LBB0_1202
	s_and_b64 vcc, exec, s[14:15]
	s_cbranch_vccz .LBB0_1205
	s_barrier
